# v66 + stick-breaking attention: touch loads pull the next key/value tile into L2 one iteration ahead
# speedup vs baseline: 1.0036x; 1.0020x over previous
.LBB0_1171:
	s_add_i32 s35, s31, s34
	s_add_u32 s29, s14, s35
	s_addc_u32 s38, s15, 0
	s_mov_b32 s100, s38
	v_mov_b32_e32 v35, s38
	v_or_b32_e32 v34, s29, v116
	v_lshlrev_b64 v[34:35], 10, v[34:35]
	v_lshl_add_u64 v[42:43], v[140:141], 0, v[34:35]
	global_load_dwordx4 v[34:37], v[42:43], off
	v_add_co_u32_e32 v44, vcc, s10, v42
	v_add_u32_e32 v167, s34, v119
	s_nop 0
	v_addc_co_u32_e32 v45, vcc, 0, v43, vcc
	global_load_dwordx4 v[38:41], v[44:45], off
	global_load_dwordx4 v[168:171], v[42:43], off offset:32
	global_load_dwordx4 v[172:175], v[44:45], off offset:32
	global_load_dwordx4 v[176:179], v[42:43], off offset:64
	global_load_dwordx4 v[180:183], v[44:45], off offset:64
	global_load_dwordx4 v[184:187], v[42:43], off offset:96
	global_load_dwordx4 v[188:191], v[44:45], off offset:96
	v_mov_b32_e32 v43, s38
	v_or_b32_e32 v42, s29, v118
	v_lshlrev_b64 v[42:43], 10, v[42:43]
	v_lshl_add_u64 v[42:43], v[142:143], 0, v[42:43]
	global_load_dwordx4 v[82:85], v[42:43], off
	v_mov_b32_e32 v43, s38
	v_or_b32_e32 v42, s29, v124
	v_lshlrev_b64 v[42:43], 10, v[42:43]
	v_lshl_add_u64 v[42:43], v[142:143], 0, v[42:43]
	global_load_dwordx4 v[86:89], v[42:43], off
	v_mov_b32_e32 v43, s38
	v_or_b32_e32 v42, s29, v126
	v_lshlrev_b64 v[42:43], 10, v[42:43]
	v_lshl_add_u64 v[42:43], v[142:143], 0, v[42:43]
	global_load_dwordx4 v[90:93], v[42:43], off
	v_mov_b32_e32 v43, s38
	v_or_b32_e32 v42, s29, v128
	v_lshlrev_b64 v[42:43], 10, v[42:43]
	v_lshl_add_u64 v[42:43], v[142:143], 0, v[42:43]
	global_load_dwordx4 v[94:97], v[42:43], off
	v_mov_b32_e32 v43, s38
	v_or_b32_e32 v42, s29, v130
	v_lshlrev_b64 v[42:43], 10, v[42:43]
	v_lshl_add_u64 v[42:43], v[142:143], 0, v[42:43]
	global_load_dwordx4 v[98:101], v[42:43], off
	v_mov_b32_e32 v43, s38
	v_or_b32_e32 v42, s29, v132
	v_lshlrev_b64 v[42:43], 10, v[42:43]
	v_lshl_add_u64 v[42:43], v[142:143], 0, v[42:43]
	global_load_dwordx4 v[102:105], v[42:43], off
	v_mov_b32_e32 v43, s38
	v_or_b32_e32 v42, s29, v134
	v_lshlrev_b64 v[42:43], 10, v[42:43]
	v_lshl_add_u64 v[42:43], v[142:143], 0, v[42:43]
	global_load_dwordx4 v[106:109], v[42:43], off
	v_mov_b32_e32 v43, s38
	s_cmp_eq_u32 s34, 0
	v_cmp_lt_u32_e64 s[38:39], v167, v125
	s_cselect_b64 vcc, -1, 0
	v_or_b32_e32 v42, s29, v136
	v_lshlrev_b64 v[42:43], 10, v[42:43]
	v_lshl_add_u64 v[42:43], v[142:143], 0, v[42:43]
	global_load_dwordx4 v[110:113], v[42:43], off
	v_mov_b32_e32 v200, 0xffff0000
	v_mov_b32_e32 v201, -1
	v_mov_b32_e32 v202, 0xffff8000
	v_mov_b32_e32 v203, -1
	v_mov_b32_e32 v245, s100
	v_or_b32_e32 v244, s29, v116
	v_lshlrev_b64 v[244:245], 10, v[244:245]
	v_lshl_add_u64 v[246:247], v[244:245], 0, v[202:203]
	v_lshl_add_u64 v[244:245], v[244:245], 0, v[200:201]
	v_lshl_add_u64 v[248:249], v[140:141], 0, v[244:245]
	global_load_dword v226, v[248:249], off
	v_lshl_add_u64 v[248:249], v[140:141], 0, v[246:247]
	global_load_dword v226, v[248:249], off
	v_lshl_add_u64 v[248:249], v[142:143], 0, v[244:245]
	global_load_dword v226, v[248:249], off
	v_lshl_add_u64 v[248:249], v[142:143], 0, v[246:247]
	global_load_dword v226, v[248:249], off
	s_mov_b32 s29, 0xd7d1fdd
	s_waitcnt vmcnt(19)
	v_mfma_f32_32x32x16_bf16 v[50:65], v[34:37], v[66:69], 0
	s_waitcnt vmcnt(11)
	ds_write_b128 v115, v[82:85]
	s_waitcnt vmcnt(10)
	ds_write_b128 v115, v[86:89] offset:1536
	s_waitcnt vmcnt(9)
	ds_write_b128 v115, v[90:93] offset:3072
	s_waitcnt vmcnt(8)
	ds_write_b128 v115, v[94:97] offset:4608
	s_waitcnt vmcnt(7)
	ds_write_b128 v115, v[98:101] offset:6144
	s_waitcnt vmcnt(6)
	ds_write_b128 v115, v[102:105] offset:7680
	s_waitcnt vmcnt(5)
	ds_write_b128 v115, v[106:109] offset:9216
	s_waitcnt vmcnt(4)
	ds_write_b128 v115, v[110:113] offset:10752
	v_mfma_f32_32x32x16_bf16 v[50:65], v[168:171], v[70:73], v[50:65]
	v_mfma_f32_32x32x16_bf16 v[50:65], v[176:179], v[74:77], v[50:65]
	v_mfma_f32_32x32x16_bf16 v[50:65], v[184:187], v[78:81], v[50:65]
	v_mfma_f32_32x32x16_bf16 v[34:49], v[38:41], v[66:69], 0
	s_nop 10
	v_max_f32_e32 v50, v50, v50
	v_min_f32_e32 v50, 0x42fc0000, v50
	v_exp_f32_e32 v50, v50
	s_nop 0
	v_add_f32_e32 v50, 1.0, v50
	v_rcp_f32_e32 v50, v50
	v_mfma_f32_32x32x16_bf16 v[34:49], v[172:175], v[70:73], v[34:49]
	v_cndmask_b32_e64 v168, 1.0, v50, s[38:39]
	v_cndmask_b32_e32 v168, v50, v168, vcc
	v_max_f32_e32 v50, v51, v51
	v_min_f32_e32 v50, 0x42fc0000, v50
	v_exp_f32_e32 v50, v50
	v_add_u32_e32 v51, 1, v167
	v_cmp_lt_u32_e64 s[38:39], v51, v125
	v_mfma_f32_32x32x16_bf16 v[34:49], v[180:183], v[74:77], v[34:49]
	v_add_f32_e32 v50, 1.0, v50
	v_rcp_f32_e32 v50, v50
	s_nop 0
	v_cndmask_b32_e64 v51, 1.0, v50, s[38:39]
	v_cndmask_b32_e32 v169, v50, v51, vcc
	v_max_f32_e32 v50, v52, v52
	v_min_f32_e32 v50, 0x42fc0000, v50
	v_exp_f32_e32 v50, v50
	v_add_u32_e32 v51, 2, v167
	v_cmp_lt_u32_e64 s[38:39], v51, v125
	v_mfma_f32_32x32x16_bf16 v[34:49], v[188:191], v[78:81], v[34:49]
	v_add_f32_e32 v50, 1.0, v50
	v_rcp_f32_e32 v50, v50
	s_nop 0
	v_cndmask_b32_e64 v51, 1.0, v50, s[38:39]
	v_cndmask_b32_e32 v52, v50, v51, vcc
	v_max_f32_e32 v50, v53, v53
	v_min_f32_e32 v50, 0x42fc0000, v50
	v_exp_f32_e32 v50, v50
	v_add_u32_e32 v51, 3, v167
	v_cmp_lt_u32_e64 s[38:39], v51, v125
	s_nop 1
	v_max_f32_e32 v34, v34, v34
	v_add_f32_e32 v50, 1.0, v50
	v_rcp_f32_e32 v50, v50
	v_min_f32_e32 v34, 0x42fc0000, v34
	v_max_f32_e32 v35, v35, v35
	v_exp_f32_e32 v34, v34
	v_cndmask_b32_e64 v51, 1.0, v50, s[38:39]
	v_cndmask_b32_e32 v53, v50, v51, vcc
	v_max_f32_e32 v50, v54, v54
	v_min_f32_e32 v50, 0x42fc0000, v50
	v_exp_f32_e32 v50, v50
	v_cmp_lt_i32_e64 s[38:39], v167, v127
	v_min_f32_e32 v35, 0x42fc0000, v35
	v_max_f32_e32 v36, v36, v36
	v_add_f32_e32 v50, 1.0, v50
	v_rcp_f32_e32 v50, v50
	v_exp_f32_e32 v35, v35
	v_min_f32_e32 v36, 0x42fc0000, v36
	v_max_f32_e32 v37, v37, v37
	v_cndmask_b32_e64 v51, 1.0, v50, s[38:39]
	v_cndmask_b32_e32 v54, v50, v51, vcc
	v_max_f32_e32 v50, v55, v55
	v_min_f32_e32 v50, 0x42fc0000, v50
	v_exp_f32_e32 v50, v50
	v_cmp_lt_i32_e64 s[38:39], v167, v129
	v_exp_f32_e32 v36, v36
	v_min_f32_e32 v37, 0x42fc0000, v37
	v_add_f32_e32 v50, 1.0, v50
	v_rcp_f32_e32 v50, v50
	v_max_f32_e32 v38, v38, v38
	v_exp_f32_e32 v37, v37
	v_min_f32_e32 v38, 0x42fc0000, v38
	v_cndmask_b32_e64 v51, 1.0, v50, s[38:39]
	v_cndmask_b32_e32 v55, v50, v51, vcc
	v_max_f32_e32 v50, v56, v56
	v_min_f32_e32 v50, 0x42fc0000, v50
	v_exp_f32_e32 v50, v50
	v_cmp_lt_i32_e64 s[38:39], v167, v131
	v_add_f32_e32 v34, 1.0, v34
	v_exp_f32_e32 v38, v38
	v_add_f32_e32 v50, 1.0, v50
	v_rcp_f32_e32 v50, v50
	v_rcp_f32_e32 v34, v34
	v_add_f32_e32 v35, 1.0, v35
	v_rcp_f32_e32 v35, v35
	v_cndmask_b32_e64 v51, 1.0, v50, s[38:39]
	v_cndmask_b32_e32 v56, v50, v51, vcc
	v_max_f32_e32 v50, v57, v57
	v_min_f32_e32 v50, 0x42fc0000, v50
	v_exp_f32_e32 v50, v50
	v_cmp_lt_i32_e64 s[38:39], v167, v133
	v_add_f32_e32 v36, 1.0, v36
	v_rcp_f32_e32 v36, v36
	v_add_f32_e32 v50, 1.0, v50
	v_rcp_f32_e32 v50, v50
	v_add_f32_e32 v37, 1.0, v37
	v_rcp_f32_e32 v37, v37
	v_add_f32_e32 v38, 1.0, v38
	v_cndmask_b32_e64 v51, 1.0, v50, s[38:39]
	v_cndmask_b32_e32 v57, v50, v51, vcc
	v_max_f32_e32 v50, v58, v58
	v_min_f32_e32 v50, 0x42fc0000, v50
	v_exp_f32_e32 v50, v50
	v_cmp_lt_i32_e64 s[38:39], v167, v135
	v_rcp_f32_e32 v38, v38
	v_add_f32_e32 v50, 1.0, v50
	v_rcp_f32_e32 v50, v50
	s_nop 0
	v_cndmask_b32_e64 v51, 1.0, v50, s[38:39]
	v_cndmask_b32_e32 v58, v50, v51, vcc
	v_max_f32_e32 v50, v59, v59
	v_min_f32_e32 v50, 0x42fc0000, v50
	v_exp_f32_e32 v50, v50
	v_cmp_lt_i32_e64 s[38:39], v167, v137
	v_add_f32_e32 v50, 1.0, v50
	v_rcp_f32_e32 v50, v50
	s_nop 0
	v_cndmask_b32_e64 v51, 1.0, v50, s[38:39]
	v_cndmask_b32_e32 v59, v50, v51, vcc
	v_max_f32_e32 v50, v60, v60
	v_min_f32_e32 v50, 0x42fc0000, v50
	v_exp_f32_e32 v50, v50
	v_cmp_lt_i32_e64 s[38:39], v167, v144
	v_add_f32_e32 v50, 1.0, v50
	v_rcp_f32_e32 v50, v50
	s_nop 0
	v_cndmask_b32_e64 v51, 1.0, v50, s[38:39]
	v_cndmask_b32_e32 v60, v50, v51, vcc
	v_max_f32_e32 v50, v61, v61
	v_min_f32_e32 v50, 0x42fc0000, v50
	v_exp_f32_e32 v50, v50
	v_cmp_lt_i32_e64 s[38:39], v167, v145
	v_add_f32_e32 v50, 1.0, v50
	v_rcp_f32_e32 v50, v50
	s_nop 0
	v_cndmask_b32_e64 v51, 1.0, v50, s[38:39]
	v_cndmask_b32_e32 v61, v50, v51, vcc
	v_max_f32_e32 v50, v62, v62
	v_min_f32_e32 v50, 0x42fc0000, v50
	v_exp_f32_e32 v50, v50
	v_cmp_lt_i32_e64 s[38:39], v167, v146
	v_add_f32_e32 v50, 1.0, v50
	v_rcp_f32_e32 v50, v50
	s_nop 0
	v_cndmask_b32_e64 v51, 1.0, v50, s[38:39]
	v_cndmask_b32_e32 v62, v50, v51, vcc
	v_max_f32_e32 v50, v63, v63
	v_min_f32_e32 v50, 0x42fc0000, v50
	v_exp_f32_e32 v50, v50
	v_cmp_lt_i32_e64 s[38:39], v167, v147
	v_add_f32_e32 v50, 1.0, v50
	v_rcp_f32_e32 v50, v50
	s_nop 0
	v_cndmask_b32_e64 v51, 1.0, v50, s[38:39]
	v_cndmask_b32_e32 v63, v50, v51, vcc
	v_max_f32_e32 v50, v64, v64
	v_min_f32_e32 v50, 0x42fc0000, v50
	v_exp_f32_e32 v50, v50
	v_cmp_lt_i32_e64 s[38:39], v167, v148
	v_add_f32_e32 v50, 1.0, v50
	v_rcp_f32_e32 v50, v50
	s_nop 0
	v_cndmask_b32_e64 v51, 1.0, v50, s[38:39]
	v_cndmask_b32_e32 v64, v50, v51, vcc
	v_max_f32_e32 v50, v65, v65
	v_min_f32_e32 v50, 0x42fc0000, v50
	v_exp_f32_e32 v50, v50
	v_cmp_lt_i32_e64 s[38:39], v167, v149
	v_add_f32_e32 v50, 1.0, v50
	v_rcp_f32_e32 v50, v50
	s_nop 0
	v_cndmask_b32_e64 v51, 1.0, v50, s[38:39]
	v_cmp_lt_i32_e64 s[38:39], v167, v150
	v_cndmask_b32_e32 v65, v50, v51, vcc
	s_nop 0
	v_cndmask_b32_e64 v50, 1.0, v34, s[38:39]
	v_cmp_lt_i32_e64 s[38:39], v167, v151
	v_cndmask_b32_e32 v34, v34, v50, vcc
	s_nop 0
	v_cndmask_b32_e64 v50, 1.0, v35, s[38:39]
	v_cmp_lt_i32_e64 s[38:39], v167, v152
	v_cndmask_b32_e32 v35, v35, v50, vcc
	s_nop 0
	v_cndmask_b32_e64 v50, 1.0, v36, s[38:39]
	v_cmp_lt_i32_e64 s[38:39], v167, v153
	v_cndmask_b32_e32 v36, v36, v50, vcc
	s_nop 0
	v_cndmask_b32_e64 v50, 1.0, v37, s[38:39]
	v_cmp_lt_i32_e64 s[38:39], v167, v154
	v_cndmask_b32_e32 v37, v37, v50, vcc
	v_mul_f32_e32 v51, v36, v37
	v_cndmask_b32_e64 v50, 1.0, v38, s[38:39]
	v_cndmask_b32_e32 v170, v38, v50, vcc
	v_max_f32_e32 v38, v39, v39
	v_min_f32_e32 v38, 0x42fc0000, v38
	v_exp_f32_e32 v38, v38
	v_cmp_lt_i32_e64 s[38:39], v167, v155
	v_add_f32_e32 v38, 1.0, v38
	v_rcp_f32_e32 v38, v38
	s_nop 0
	v_cndmask_b32_e64 v39, 1.0, v38, s[38:39]
	v_cndmask_b32_e32 v171, v38, v39, vcc
	v_max_f32_e32 v38, v40, v40
	v_min_f32_e32 v38, 0x42fc0000, v38
	v_exp_f32_e32 v38, v38
	v_cmp_lt_i32_e64 s[38:39], v167, v156
	v_mul_f32_e32 v177, v170, v171
	v_mul_f32_e32 v40, v56, v57
	v_add_f32_e32 v38, 1.0, v38
	v_rcp_f32_e32 v38, v38
	s_nop 0
	v_cndmask_b32_e64 v39, 1.0, v38, s[38:39]
	v_cndmask_b32_e32 v172, v38, v39, vcc
	v_max_f32_e32 v38, v41, v41
	v_min_f32_e32 v38, 0x42fc0000, v38
	v_exp_f32_e32 v38, v38
	v_cmp_lt_i32_e64 s[38:39], v167, v157
	v_mul_f32_e32 v41, v58, v59
	v_add_f32_e32 v38, 1.0, v38
	v_rcp_f32_e32 v38, v38
	s_nop 0
	v_cndmask_b32_e64 v39, 1.0, v38, s[38:39]
	v_cndmask_b32_e32 v173, v38, v39, vcc
	v_max_f32_e32 v38, v42, v42
	v_min_f32_e32 v38, 0x42fc0000, v38
	v_exp_f32_e32 v38, v38
	v_cmp_lt_i32_e64 s[38:39], v167, v158
	v_mul_f32_e32 v178, v172, v173
	v_mul_f32_e32 v177, v177, v178
	v_add_f32_e32 v38, 1.0, v38
	v_rcp_f32_e32 v38, v38
	v_mov_b32_e32 v178, v177
	s_nop 1
	v_permlane32_swap_b32_e32 v177, v178
	v_cndmask_b32_e64 v39, 1.0, v38, s[38:39]
	v_cndmask_b32_e32 v42, v38, v39, vcc
	v_max_f32_e32 v38, v43, v43
	v_min_f32_e32 v38, 0x42fc0000, v38
	v_exp_f32_e32 v38, v38
	v_cmp_lt_i32_e64 s[38:39], v167, v159
	v_add_f32_e32 v38, 1.0, v38
	v_rcp_f32_e32 v38, v38
	s_nop 0
	v_cndmask_b32_e64 v39, 1.0, v38, s[38:39]
	v_cndmask_b32_e32 v43, v38, v39, vcc
	v_max_f32_e32 v38, v44, v44
	v_min_f32_e32 v38, 0x42fc0000, v38
	v_exp_f32_e32 v38, v38
	v_cmp_lt_i32_e64 s[38:39], v167, v160
	v_mul_f32_e32 v179, v42, v43
	v_sub_f32_e32 v42, 1.0, v42
	v_add_f32_e32 v38, 1.0, v38
	v_rcp_f32_e32 v38, v38
	s_nop 0
	v_cndmask_b32_e64 v39, 1.0, v38, s[38:39]
	v_cndmask_b32_e32 v44, v38, v39, vcc
	v_max_f32_e32 v38, v45, v45
	v_min_f32_e32 v38, 0x42fc0000, v38
	v_exp_f32_e32 v38, v38
	v_cmp_lt_i32_e64 s[38:39], v167, v161
	v_add_f32_e32 v38, 1.0, v38
	v_rcp_f32_e32 v38, v38
	s_nop 0
	v_cndmask_b32_e64 v39, 1.0, v38, s[38:39]
	v_cndmask_b32_e32 v45, v38, v39, vcc
	v_max_f32_e32 v38, v46, v46
	v_min_f32_e32 v38, 0x42fc0000, v38
	v_exp_f32_e32 v38, v38
	v_cmp_lt_i32_e64 s[38:39], v167, v162
	v_mul_f32_e32 v180, v44, v45
	v_mul_f32_e32 v179, v179, v180
	v_add_f32_e32 v38, 1.0, v38
	v_rcp_f32_e32 v38, v38
	v_mov_b32_e32 v180, v179
	s_nop 1
	v_permlane32_swap_b32_e32 v179, v180
	v_cndmask_b32_e64 v39, 1.0, v38, s[38:39]
	v_cndmask_b32_e32 v174, v38, v39, vcc
	v_max_f32_e32 v38, v47, v47
	v_min_f32_e32 v38, 0x42fc0000, v38
	v_exp_f32_e32 v38, v38
	v_cmp_lt_i32_e64 s[38:39], v167, v163
	v_mul_f32_e32 v47, v62, v63
	v_mul_f32_e32 v46, v60, v61
	v_add_f32_e32 v38, 1.0, v38
	v_rcp_f32_e32 v38, v38
	v_mul_f32_e32 v41, v41, v46
	v_mov_b32_e32 v46, v41
	s_nop 1
	v_permlane32_swap_b32_e32 v41, v46
	v_cndmask_b32_e64 v39, 1.0, v38, s[38:39]
	v_cndmask_b32_e32 v175, v38, v39, vcc
	v_max_f32_e32 v38, v48, v48
	v_min_f32_e32 v38, 0x42fc0000, v38
	v_exp_f32_e32 v38, v38
	v_cmp_lt_i32_e64 s[38:39], v167, v164
	v_mul_f32_e32 v181, v174, v175
	v_mul_f32_e32 v48, v64, v65
	v_add_f32_e32 v38, 1.0, v38
	v_rcp_f32_e32 v38, v38
	v_mul_f32_e32 v47, v47, v48
	v_mov_b32_e32 v48, v47
	s_nop 1
	v_permlane32_swap_b32_e32 v47, v48
	v_cndmask_b32_e64 v39, 1.0, v38, s[38:39]
	v_cndmask_b32_e32 v176, v38, v39, vcc
	v_max_f32_e32 v38, v49, v49
	v_min_f32_e32 v38, 0x42fc0000, v38
	v_exp_f32_e32 v38, v38
	v_cmp_lt_i32_e64 s[38:39], v167, v165
	v_mul_f32_e32 v49, v34, v35
	v_mul_f32_e32 v49, v49, v51
	v_add_f32_e32 v38, 1.0, v38
	v_rcp_f32_e32 v38, v38
	v_mov_b32_e32 v51, v49
	s_nop 1
	v_permlane32_swap_b32_e32 v49, v51
	v_cndmask_b32_e64 v39, 1.0, v38, s[38:39]
	v_cndmask_b32_e32 v167, v38, v39, vcc
	v_mul_f32_e32 v182, v176, v167
	v_mul_f32_e32 v181, v181, v182
	v_mov_b32_e32 v182, v181
	s_nop 1
	v_permlane32_swap_b32_e32 v181, v182
	v_mul_f32_e32 v182, v166, v182
	v_mul_f32_e32 v181, v182, v181
	v_mul_f32_e32 v180, v181, v180
	v_mul_f32_e32 v179, v180, v179
	v_mul_f32_e32 v178, v179, v178
	v_mul_f32_e32 v177, v178, v177
	v_mul_f32_e32 v51, v177, v51
	v_mul_f32_e32 v38, v168, v169
	v_mul_f32_e32 v39, v52, v53
	v_mul_f32_e32 v49, v51, v49
	v_mul_f32_e32 v50, v38, v39
	v_mul_f32_e32 v39, v54, v55
	v_mul_f32_e32 v48, v49, v48
	v_mul_f32_e32 v39, v39, v40
	v_mul_f32_e32 v47, v48, v47
	v_mov_b32_e32 v40, v39
	v_mul_f32_e32 v46, v47, v46
	s_nop 0
	v_permlane32_swap_b32_e32 v39, v40
	v_mul_f32_e32 v41, v46, v41
	v_mov_b32_e32 v38, v50
	v_mul_f32_e32 v40, v41, v40
	s_nop 0
	v_permlane32_swap_b32_e32 v50, v38
	v_mul_f32_e32 v39, v40, v39
	v_cndmask_b32_e64 v177, v177, v51, s[36:37]
	v_mul_f32_e32 v51, v39, v38
	v_cndmask_b32_e64 v38, v39, v51, s[36:37]
	v_mul_f32_e32 v39, v53, v38
	v_cndmask_b32_e64 v40, v41, v40, s[36:37]
	v_mul_f32_e32 v41, v52, v39
	v_cndmask_b32_e64 v180, v181, v180, s[36:37]
	v_cndmask_b32_e64 v181, v47, v46, s[36:37]
	v_mul_f32_e32 v46, v169, v41
	v_sub_f32_e32 v47, 1.0, v168
	v_mul_f32_e32 v46, v47, v46
	v_sub_f32_e32 v47, 1.0, v169
	v_mul_f32_e32 v41, v47, v41
	v_sub_f32_e32 v47, 1.0, v52
	v_mul_f32_e32 v39, v47, v39
	v_sub_f32_e32 v47, 1.0, v53
	v_mul_f32_e32 v38, v47, v38
	v_mul_f32_e32 v47, v57, v40
	v_cndmask_b32_e64 v178, v179, v178, s[36:37]
	v_cndmask_b32_e64 v179, v49, v48, s[36:37]
	v_mul_f32_e32 v48, v56, v47
	v_mul_f32_e32 v49, v55, v48
	v_sub_f32_e32 v52, 1.0, v54
	v_mul_f32_e32 v49, v52, v49
	v_sub_f32_e32 v52, 1.0, v55
	v_mul_f32_e32 v48, v52, v48
	v_sub_f32_e32 v52, 1.0, v56
	v_mul_f32_e32 v52, v52, v47
	v_sub_f32_e32 v47, 1.0, v57
	v_mul_f32_e32 v40, v47, v40
	v_cvt_pk_bf16_f32 v47, v39, v38
	v_mul_f32_e32 v38, v61, v181
	v_mul_f32_e32 v39, v60, v38
	v_cvt_pk_bf16_f32 v46, v46, v41
	v_cvt_pk_bf16_f32 v48, v49, v48
	v_cvt_pk_bf16_f32 v49, v52, v40
	v_mul_f32_e32 v40, v59, v39
	v_sub_f32_e32 v41, 1.0, v58
	v_mul_f32_e32 v40, v41, v40
	v_sub_f32_e32 v41, 1.0, v59
	v_mul_f32_e32 v39, v41, v39
	v_sub_f32_e32 v41, 1.0, v60
	v_mul_f32_e32 v41, v41, v38
	v_sub_f32_e32 v38, 1.0, v61
	v_mul_f32_e32 v52, v38, v181
	v_mul_f32_e32 v38, v65, v179
	v_mul_f32_e32 v53, v64, v38
	v_mul_f32_e32 v54, v63, v53
	v_sub_f32_e32 v55, 1.0, v62
	v_mul_f32_e32 v54, v55, v54
	v_sub_f32_e32 v55, 1.0, v63
	v_mul_f32_e32 v53, v55, v53
	v_sub_f32_e32 v55, 1.0, v64
	v_mul_f32_e32 v55, v55, v38
	v_sub_f32_e32 v38, 1.0, v65
	v_mul_f32_e32 v56, v38, v179
	v_cvt_pk_bf16_f32 v38, v40, v39
	v_cvt_pk_bf16_f32 v39, v41, v52
	v_mul_f32_e32 v52, v37, v177
	v_cvt_pk_bf16_f32 v40, v54, v53
	v_mul_f32_e32 v53, v36, v52
	v_sub_f32_e32 v36, 1.0, v36
	v_mul_f32_e32 v54, v35, v53
	v_sub_f32_e32 v35, 1.0, v35
	v_mul_f32_e32 v36, v36, v52
	v_mul_f32_e32 v52, v173, v178
	v_sub_f32_e32 v34, 1.0, v34
	v_mul_f32_e32 v35, v35, v53
	v_mul_f32_e32 v53, v172, v52
	v_cvt_pk_bf16_f32 v41, v55, v56
	v_mul_f32_e32 v34, v34, v54
	v_mul_f32_e32 v54, v171, v53
	v_sub_f32_e32 v55, 1.0, v170
	v_mul_f32_e32 v54, v55, v54
	v_sub_f32_e32 v55, 1.0, v171
	v_mul_f32_e32 v53, v55, v53
	v_sub_f32_e32 v55, 1.0, v172
	v_sub_f32_e32 v37, 1.0, v37
	v_mul_f32_e32 v52, v55, v52
	v_sub_f32_e32 v55, 1.0, v173
	v_mul_f32_e32 v37, v37, v177
	v_mul_f32_e32 v55, v55, v178
	v_cvt_pk_bf16_f32 v34, v34, v35
	v_cvt_pk_bf16_f32 v35, v36, v37
	v_cvt_pk_bf16_f32 v37, v52, v55
	v_mul_f32_e32 v52, v45, v180
	v_cndmask_b32_e64 v166, v166, v182, s[36:37]
	v_cvt_pk_bf16_f32 v36, v54, v53
	v_mul_f32_e32 v53, v44, v52
	v_sub_f32_e32 v44, 1.0, v44
	v_mul_f32_e32 v54, v43, v53
	v_sub_f32_e32 v43, 1.0, v43
	v_mul_f32_e32 v44, v44, v52
	v_mul_f32_e32 v52, v167, v166
	v_mul_f32_e32 v43, v43, v53
	v_mul_f32_e32 v53, v176, v52
	v_mul_f32_e32 v42, v42, v54
	v_mul_f32_e32 v54, v175, v53
	v_sub_f32_e32 v55, 1.0, v174
	v_mul_f32_e32 v54, v55, v54
	v_sub_f32_e32 v55, 1.0, v175
	v_mul_f32_e32 v53, v55, v53
	v_sub_f32_e32 v55, 1.0, v176
	v_sub_f32_e32 v45, 1.0, v45
	v_mul_f32_e32 v52, v55, v52
	v_sub_f32_e32 v55, 1.0, v167
	v_mul_f32_e32 v45, v45, v180
	v_mul_f32_e32 v55, v55, v166
	v_cvt_pk_bf16_f32 v42, v42, v43
	v_cvt_pk_bf16_f32 v43, v44, v45
	v_cvt_pk_bf16_f32 v44, v54, v53
	v_cvt_pk_bf16_f32 v45, v52, v55
	v_mul_f32_e32 v166, v51, v50
	ds_read_b64_tr_b16 v[50:51], v117
	ds_read_b64_tr_b16 v[52:53], v117 offset:1536
	ds_read_b64_tr_b16 v[54:55], v117 offset:3072
	ds_read_b64_tr_b16 v[56:57], v117 offset:4608
	ds_read_b64_tr_b16 v[58:59], v117 offset:6144
	ds_read_b64_tr_b16 v[60:61], v117 offset:7680
	ds_read_b64_tr_b16 v[62:63], v117 offset:9216
	ds_read_b64_tr_b16 v[64:65], v117 offset:10752
	s_waitcnt lgkmcnt(0)
	s_nop 0
	v_mfma_f32_32x32x16_bf16 v[18:33], v[50:53], v[46:49], v[18:33]
	v_cmp_gt_f32_e32 vcc, s29, v166
	s_cmp_lg_u64 vcc, exec
	s_cselect_b64 s[38:39], -1, 0
	s_cmp_lg_u32 s35, 0
	s_cselect_b64 s[40:41], -1, 0
	s_and_b64 s[38:39], s[40:41], s[38:39]
	s_sub_i32 s34, s34, 64
	v_mfma_f32_32x32x16_bf16 v[18:33], v[54:57], v[38:41], v[18:33]
	s_and_b64 vcc, exec, s[38:39]
	v_mfma_f32_32x32x16_bf16 v[18:33], v[58:61], v[34:37], v[18:33]
	v_mfma_f32_32x32x16_bf16 v[18:33], v[62:65], v[42:45], v[18:33]
	ds_read_b64_tr_b16 v[62:63], v117 offset:64
	ds_read_b64_tr_b16 v[64:65], v117 offset:1600
	ds_read_b64_tr_b16 v[58:59], v117 offset:3136
	ds_read_b64_tr_b16 v[60:61], v117 offset:4672
	ds_read_b64_tr_b16 v[50:51], v117 offset:6208
	ds_read_b64_tr_b16 v[52:53], v117 offset:7744
	ds_read_b64_tr_b16 v[54:55], v117 offset:9280
	ds_read_b64_tr_b16 v[56:57], v117 offset:10816
	s_waitcnt lgkmcnt(0)
	s_nop 0
	v_mfma_f32_32x32x16_bf16 v[2:17], v[62:65], v[46:49], v[2:17]
	v_mfma_f32_32x32x16_bf16 v[2:17], v[58:61], v[38:41], v[2:17]
	v_mfma_f32_32x32x16_bf16 v[2:17], v[50:53], v[34:37], v[2:17]
	v_mfma_f32_32x32x16_bf16 v[2:17], v[54:57], v[42:45], v[2:17]
	s_cbranch_vccnz .LBB0_1171
	v_lshlrev_b32_e32 v34, 1, v114
	v_mov_b32_e32 v35, v1
	v_lshl_add_u64 v[34:35], v[138:139], 0, v[34:35]
	v_cvt_pk_bf16_f32 v18, v18, v19
	v_cvt_pk_bf16_f32 v19, v20, v21
	s_nop 5
	v_cvt_pk_bf16_f32 v2, v2, v3
	v_cvt_pk_bf16_f32 v3, v4, v5
	global_store_dwordx2 v[34:35], v[18:19], off sc1
	global_store_dwordx2 v[34:35], v[2:3], off offset:64 sc1
	v_cvt_pk_bf16_f32 v2, v22, v23
	v_cvt_pk_bf16_f32 v3, v24, v25
	v_cvt_pk_bf16_f32 v4, v6, v7
	v_cvt_pk_bf16_f32 v5, v8, v9
	global_store_dwordx2 v[34:35], v[2:3], off offset:16 sc1
	global_store_dwordx2 v[34:35], v[4:5], off offset:80 sc1
	v_cvt_pk_bf16_f32 v2, v26, v27
	v_cvt_pk_bf16_f32 v3, v28, v29
	v_cvt_pk_bf16_f32 v4, v10, v11
	v_cvt_pk_bf16_f32 v5, v12, v13
	s_add_i32 s17, s17, s72
	s_add_i32 s16, s16, s72
	global_store_dwordx2 v[34:35], v[2:3], off offset:32 sc1
	global_store_dwordx2 v[34:35], v[4:5], off offset:96 sc1
	v_cvt_pk_bf16_f32 v2, v30, v31
	v_cvt_pk_bf16_f32 v3, v32, v33
	v_cvt_pk_bf16_f32 v4, v14, v15
	v_cvt_pk_bf16_f32 v5, v16, v17
	s_cmpk_lt_i32 s17, 0x1000
	global_store_dwordx2 v[34:35], v[2:3], off offset:48 sc1
	global_store_dwordx2 v[34:35], v[4:5], off offset:112 sc1
	s_cbranch_scc1 .LBB0_1170
